# P0 calibration: six tensors' 48 sample loads through one 24-deep rolling window, six DPP wave sums, one barrier pair (was 6 x load/reduce/2 barriers); attention PV per-operand lgkmcnt waits
# speedup vs baseline: 1.0064x; 1.0064x over previous
.LBB0_35:
	v_mov_b32_e32 v234, v66
	v_lshlrev_b32_e32 v213, 4, v66
	v_add_u32_e32 v214, 0x2000, v213
	v_readlane_b32 s80, v254, 20
	v_readlane_b32 s81, v254, 21
	s_mov_b64 s[82:83], s[80:81]
	global_load_dwordx4 v[36:39], v213, s[82:83]
	global_load_dwordx4 v[40:43], v214, s[82:83]
	s_add_u32 s82, s82, 0xc00000
	s_addc_u32 s83, s83, 0
	global_load_dwordx4 v[44:47], v213, s[82:83]
	global_load_dwordx4 v[48:51], v214, s[82:83]
	s_add_u32 s82, s82, 0xc00000
	s_addc_u32 s83, s83, 0
	global_load_dwordx4 v[52:55], v213, s[82:83]
	global_load_dwordx4 v[56:59], v214, s[82:83]
	s_add_u32 s82, s82, 0xc00000
	s_addc_u32 s83, s83, 0
	global_load_dwordx4 v[60:63], v213, s[82:83]
	global_load_dwordx4 v[64:67], v214, s[82:83]
	v_readlane_b32 s80, v254, 26
	v_readlane_b32 s81, v254, 27
	s_mov_b64 s[82:83], s[80:81]
	global_load_dwordx4 v[176:179], v213, s[82:83]
	global_load_dwordx4 v[180:183], v214, s[82:83]
	s_add_u32 s82, s82, 0xb00000
	s_addc_u32 s83, s83, 0
	global_load_dwordx4 v[184:187], v213, s[82:83]
	global_load_dwordx4 v[188:191], v214, s[82:83]
	s_add_u32 s82, s82, 0xb00000
	s_addc_u32 s83, s83, 0
	global_load_dwordx4 v[192:195], v213, s[82:83]
	global_load_dwordx4 v[196:199], v214, s[82:83]
	s_add_u32 s82, s82, 0xb00000
	s_addc_u32 s83, s83, 0
	global_load_dwordx4 v[200:203], v213, s[82:83]
	global_load_dwordx4 v[204:207], v214, s[82:83]
	v_readlane_b32 s80, v254, 28
	v_readlane_b32 s81, v254, 29
	s_mov_b64 s[82:83], s[80:81]
	global_load_dwordx4 v[208:211], v213, s[82:83]
	global_load_dwordx4 v[222:225], v214, s[82:83]
	s_add_u32 s82, s82, 0xb00000
	s_addc_u32 s83, s83, 0
	global_load_dwordx4 v[226:229], v213, s[82:83]
	global_load_dwordx4 v[230:233], v214, s[82:83]
	s_add_u32 s82, s82, 0xb00000
	s_addc_u32 s83, s83, 0
	global_load_dwordx4 v[238:241], v213, s[82:83]
	global_load_dwordx4 v[242:245], v214, s[82:83]
	s_add_u32 s82, s82, 0xb00000
	s_addc_u32 s83, s83, 0
	global_load_dwordx4 v[246:249], v213, s[82:83]
	global_load_dwordx4 v[250:253], v214, s[82:83]
	s_waitcnt vmcnt(23)
	v_mul_f32_e32 v35, v37, v37
	v_mul_f32_e32 v212, v39, v39
	v_fmac_f32_e32 v35, v36, v36
	v_fmac_f32_e32 v212, v38, v38
	v_add_f32_e32 v19, v35, v212
	v_readlane_b32 s80, v254, 32
	v_readlane_b32 s81, v254, 33
	s_mov_b64 s[82:83], s[80:81]
	global_load_dwordx4 v[36:39], v213, s[82:83]
	s_waitcnt vmcnt(23)
	v_mul_f32_e32 v35, v41, v41
	v_mul_f32_e32 v212, v43, v43
	v_fmac_f32_e32 v35, v40, v40
	v_fmac_f32_e32 v212, v42, v42
	v_add_f32_e32 v35, v35, v212
	v_add_f32_e32 v19, v19, v35
	global_load_dwordx4 v[40:43], v214, s[82:83]
	s_waitcnt vmcnt(23)
	v_mul_f32_e32 v35, v45, v45
	v_mul_f32_e32 v212, v47, v47
	v_fmac_f32_e32 v35, v44, v44
	v_fmac_f32_e32 v212, v46, v46
	v_add_f32_e32 v35, v35, v212
	v_add_f32_e32 v19, v19, v35
	s_add_u32 s82, s82, 0xc00000
	s_addc_u32 s83, s83, 0
	global_load_dwordx4 v[44:47], v213, s[82:83]
	s_waitcnt vmcnt(23)
	v_mul_f32_e32 v35, v49, v49
	v_mul_f32_e32 v212, v51, v51
	v_fmac_f32_e32 v35, v48, v48
	v_fmac_f32_e32 v212, v50, v50
	v_add_f32_e32 v35, v35, v212
	v_add_f32_e32 v19, v19, v35
	global_load_dwordx4 v[48:51], v214, s[82:83]
	s_waitcnt vmcnt(23)
	v_mul_f32_e32 v35, v53, v53
	v_mul_f32_e32 v212, v55, v55
	v_fmac_f32_e32 v35, v52, v52
	v_fmac_f32_e32 v212, v54, v54
	v_add_f32_e32 v35, v35, v212
	v_add_f32_e32 v19, v19, v35
	s_add_u32 s82, s82, 0xc00000
	s_addc_u32 s83, s83, 0
	global_load_dwordx4 v[52:55], v213, s[82:83]
	s_waitcnt vmcnt(23)
	v_mul_f32_e32 v35, v57, v57
	v_mul_f32_e32 v212, v59, v59
	v_fmac_f32_e32 v35, v56, v56
	v_fmac_f32_e32 v212, v58, v58
	v_add_f32_e32 v35, v35, v212
	v_add_f32_e32 v19, v19, v35
	global_load_dwordx4 v[56:59], v214, s[82:83]
	s_waitcnt vmcnt(23)
	v_mul_f32_e32 v35, v61, v61
	v_mul_f32_e32 v212, v63, v63
	v_fmac_f32_e32 v35, v60, v60
	v_fmac_f32_e32 v212, v62, v62
	v_add_f32_e32 v35, v35, v212
	v_add_f32_e32 v19, v19, v35
	s_add_u32 s82, s82, 0xc00000
	s_addc_u32 s83, s83, 0
	global_load_dwordx4 v[60:63], v213, s[82:83]
	s_waitcnt vmcnt(23)
	v_mul_f32_e32 v35, v65, v65
	v_mul_f32_e32 v212, v67, v67
	v_fmac_f32_e32 v35, v64, v64
	v_fmac_f32_e32 v212, v66, v66
	v_add_f32_e32 v35, v35, v212
	v_add_f32_e32 v19, v19, v35
	global_load_dwordx4 v[64:67], v214, s[82:83]
	s_waitcnt vmcnt(23)
	v_mul_f32_e32 v35, v177, v177
	v_mul_f32_e32 v212, v179, v179
	v_fmac_f32_e32 v35, v176, v176
	v_fmac_f32_e32 v212, v178, v178
	v_add_f32_e32 v28, v35, v212
	s_mov_b64 s[82:83], s[64:65]
	global_load_dwordx4 v[176:179], v213, s[82:83]
	s_waitcnt vmcnt(23)
	v_mul_f32_e32 v35, v181, v181
	v_mul_f32_e32 v212, v183, v183
	v_fmac_f32_e32 v35, v180, v180
	v_fmac_f32_e32 v212, v182, v182
	v_add_f32_e32 v35, v35, v212
	v_add_f32_e32 v28, v28, v35
	global_load_dwordx4 v[180:183], v214, s[82:83]
	s_waitcnt vmcnt(23)
	v_mul_f32_e32 v35, v185, v185
	v_mul_f32_e32 v212, v187, v187
	v_fmac_f32_e32 v35, v184, v184
	v_fmac_f32_e32 v212, v186, v186
	v_add_f32_e32 v35, v35, v212
	v_add_f32_e32 v28, v28, v35
	s_add_u32 s82, s82, 0x7000000
	s_addc_u32 s83, s83, 0
	global_load_dwordx4 v[184:187], v213, s[82:83]
	s_waitcnt vmcnt(23)
	v_mul_f32_e32 v35, v189, v189
	v_mul_f32_e32 v212, v191, v191
	v_fmac_f32_e32 v35, v188, v188
	v_fmac_f32_e32 v212, v190, v190
	v_add_f32_e32 v35, v35, v212
	v_add_f32_e32 v28, v28, v35
	global_load_dwordx4 v[188:191], v214, s[82:83]
	s_waitcnt vmcnt(23)
	v_mul_f32_e32 v35, v193, v193
	v_mul_f32_e32 v212, v195, v195
	v_fmac_f32_e32 v35, v192, v192
	v_fmac_f32_e32 v212, v194, v194
	v_add_f32_e32 v35, v35, v212
	v_add_f32_e32 v28, v28, v35
	s_add_u32 s82, s82, 0x7000000
	s_addc_u32 s83, s83, 0
	global_load_dwordx4 v[192:195], v213, s[82:83]
	s_waitcnt vmcnt(23)
	v_mul_f32_e32 v35, v197, v197
	v_mul_f32_e32 v212, v199, v199
	v_fmac_f32_e32 v35, v196, v196
	v_fmac_f32_e32 v212, v198, v198
	v_add_f32_e32 v35, v35, v212
	v_add_f32_e32 v28, v28, v35
	global_load_dwordx4 v[196:199], v214, s[82:83]
	s_waitcnt vmcnt(23)
	v_mul_f32_e32 v35, v201, v201
	v_mul_f32_e32 v212, v203, v203
	v_fmac_f32_e32 v35, v200, v200
	v_fmac_f32_e32 v212, v202, v202
	v_add_f32_e32 v35, v35, v212
	v_add_f32_e32 v28, v28, v35
	s_add_u32 s82, s82, 0x7000000
	s_addc_u32 s83, s83, 0
	global_load_dwordx4 v[200:203], v213, s[82:83]
	s_waitcnt vmcnt(23)
	v_mul_f32_e32 v35, v205, v205
	v_mul_f32_e32 v212, v207, v207
	v_fmac_f32_e32 v35, v204, v204
	v_fmac_f32_e32 v212, v206, v206
	v_add_f32_e32 v35, v35, v212
	v_add_f32_e32 v28, v28, v35
	global_load_dwordx4 v[204:207], v214, s[82:83]
	s_waitcnt vmcnt(23)
	v_mul_f32_e32 v35, v209, v209
	v_mul_f32_e32 v212, v211, v211
	v_fmac_f32_e32 v35, v208, v208
	v_fmac_f32_e32 v212, v210, v210
	v_add_f32_e32 v29, v35, v212
	s_mov_b64 s[82:83], s[66:67]
	global_load_dwordx4 v[208:211], v213, s[82:83]
	s_waitcnt vmcnt(23)
	v_mul_f32_e32 v35, v223, v223
	v_mul_f32_e32 v212, v225, v225
	v_fmac_f32_e32 v35, v222, v222
	v_fmac_f32_e32 v212, v224, v224
	v_add_f32_e32 v35, v35, v212
	v_add_f32_e32 v29, v29, v35
	global_load_dwordx4 v[222:225], v214, s[82:83]
	s_waitcnt vmcnt(23)
	v_mul_f32_e32 v35, v227, v227
	v_mul_f32_e32 v212, v229, v229
	v_fmac_f32_e32 v35, v226, v226
	v_fmac_f32_e32 v212, v228, v228
	v_add_f32_e32 v35, v35, v212
	v_add_f32_e32 v29, v29, v35
	s_add_u32 s82, s82, 0x7000000
	s_addc_u32 s83, s83, 0
	global_load_dwordx4 v[226:229], v213, s[82:83]
	s_waitcnt vmcnt(23)
	v_mul_f32_e32 v35, v231, v231
	v_mul_f32_e32 v212, v233, v233
	v_fmac_f32_e32 v35, v230, v230
	v_fmac_f32_e32 v212, v232, v232
	v_add_f32_e32 v35, v35, v212
	v_add_f32_e32 v29, v29, v35
	global_load_dwordx4 v[230:233], v214, s[82:83]
	s_waitcnt vmcnt(23)
	v_mul_f32_e32 v35, v239, v239
	v_mul_f32_e32 v212, v241, v241
	v_fmac_f32_e32 v35, v238, v238
	v_fmac_f32_e32 v212, v240, v240
	v_add_f32_e32 v35, v35, v212
	v_add_f32_e32 v29, v29, v35
	s_add_u32 s82, s82, 0x7000000
	s_addc_u32 s83, s83, 0
	global_load_dwordx4 v[238:241], v213, s[82:83]
	s_waitcnt vmcnt(23)
	v_mul_f32_e32 v35, v243, v243
	v_mul_f32_e32 v212, v245, v245
	v_fmac_f32_e32 v35, v242, v242
	v_fmac_f32_e32 v212, v244, v244
	v_add_f32_e32 v35, v35, v212
	v_add_f32_e32 v29, v29, v35
	global_load_dwordx4 v[242:245], v214, s[82:83]
	s_waitcnt vmcnt(23)
	v_mul_f32_e32 v35, v247, v247
	v_mul_f32_e32 v212, v249, v249
	v_fmac_f32_e32 v35, v246, v246
	v_fmac_f32_e32 v212, v248, v248
	v_add_f32_e32 v35, v35, v212
	v_add_f32_e32 v29, v29, v35
	s_add_u32 s82, s82, 0x7000000
	s_addc_u32 s83, s83, 0
	global_load_dwordx4 v[246:249], v213, s[82:83]
	s_waitcnt vmcnt(23)
	v_mul_f32_e32 v35, v251, v251
	v_mul_f32_e32 v212, v253, v253
	v_fmac_f32_e32 v35, v250, v250
	v_fmac_f32_e32 v212, v252, v252
	v_add_f32_e32 v35, v35, v212
	v_add_f32_e32 v29, v29, v35
	global_load_dwordx4 v[250:253], v214, s[82:83]
	s_waitcnt vmcnt(23)
	v_mul_f32_e32 v35, v37, v37
	v_mul_f32_e32 v212, v39, v39
	v_fmac_f32_e32 v35, v36, v36
	v_fmac_f32_e32 v212, v38, v38
	v_add_f32_e32 v30, v35, v212
	s_waitcnt vmcnt(22)
	v_mul_f32_e32 v35, v41, v41
	v_mul_f32_e32 v212, v43, v43
	v_fmac_f32_e32 v35, v40, v40
	v_fmac_f32_e32 v212, v42, v42
	v_add_f32_e32 v35, v35, v212
	v_add_f32_e32 v30, v30, v35
	s_waitcnt vmcnt(21)
	v_mul_f32_e32 v35, v45, v45
	v_mul_f32_e32 v212, v47, v47
	v_fmac_f32_e32 v35, v44, v44
	v_fmac_f32_e32 v212, v46, v46
	v_add_f32_e32 v35, v35, v212
	v_add_f32_e32 v30, v30, v35
	s_waitcnt vmcnt(20)
	v_mul_f32_e32 v35, v49, v49
	v_mul_f32_e32 v212, v51, v51
	v_fmac_f32_e32 v35, v48, v48
	v_fmac_f32_e32 v212, v50, v50
	v_add_f32_e32 v35, v35, v212
	v_add_f32_e32 v30, v30, v35
	s_waitcnt vmcnt(19)
	v_mul_f32_e32 v35, v53, v53
	v_mul_f32_e32 v212, v55, v55
	v_fmac_f32_e32 v35, v52, v52
	v_fmac_f32_e32 v212, v54, v54
	v_add_f32_e32 v35, v35, v212
	v_add_f32_e32 v30, v30, v35
	s_waitcnt vmcnt(18)
	v_mul_f32_e32 v35, v57, v57
	v_mul_f32_e32 v212, v59, v59
	v_fmac_f32_e32 v35, v56, v56
	v_fmac_f32_e32 v212, v58, v58
	v_add_f32_e32 v35, v35, v212
	v_add_f32_e32 v30, v30, v35
	s_waitcnt vmcnt(17)
	v_mul_f32_e32 v35, v61, v61
	v_mul_f32_e32 v212, v63, v63
	v_fmac_f32_e32 v35, v60, v60
	v_fmac_f32_e32 v212, v62, v62
	v_add_f32_e32 v35, v35, v212
	v_add_f32_e32 v30, v30, v35
	s_waitcnt vmcnt(16)
	v_mul_f32_e32 v35, v65, v65
	v_mul_f32_e32 v212, v67, v67
	v_fmac_f32_e32 v35, v64, v64
	v_fmac_f32_e32 v212, v66, v66
	v_add_f32_e32 v35, v35, v212
	v_add_f32_e32 v30, v30, v35
	s_waitcnt vmcnt(15)
	v_mul_f32_e32 v35, v177, v177
	v_mul_f32_e32 v212, v179, v179
	v_fmac_f32_e32 v35, v176, v176
	v_fmac_f32_e32 v212, v178, v178
	v_add_f32_e32 v31, v35, v212
	s_waitcnt vmcnt(14)
	v_mul_f32_e32 v35, v181, v181
	v_mul_f32_e32 v212, v183, v183
	v_fmac_f32_e32 v35, v180, v180
	v_fmac_f32_e32 v212, v182, v182
	v_add_f32_e32 v35, v35, v212
	v_add_f32_e32 v31, v31, v35
	s_waitcnt vmcnt(13)
	v_mul_f32_e32 v35, v185, v185
	v_mul_f32_e32 v212, v187, v187
	v_fmac_f32_e32 v35, v184, v184
	v_fmac_f32_e32 v212, v186, v186
	v_add_f32_e32 v35, v35, v212
	v_add_f32_e32 v31, v31, v35
	s_waitcnt vmcnt(12)
	v_mul_f32_e32 v35, v189, v189
	v_mul_f32_e32 v212, v191, v191
	v_fmac_f32_e32 v35, v188, v188
	v_fmac_f32_e32 v212, v190, v190
	v_add_f32_e32 v35, v35, v212
	v_add_f32_e32 v31, v31, v35
	s_waitcnt vmcnt(11)
	v_mul_f32_e32 v35, v193, v193
	v_mul_f32_e32 v212, v195, v195
	v_fmac_f32_e32 v35, v192, v192
	v_fmac_f32_e32 v212, v194, v194
	v_add_f32_e32 v35, v35, v212
	v_add_f32_e32 v31, v31, v35
	s_waitcnt vmcnt(10)
	v_mul_f32_e32 v35, v197, v197
	v_mul_f32_e32 v212, v199, v199
	v_fmac_f32_e32 v35, v196, v196
	v_fmac_f32_e32 v212, v198, v198
	v_add_f32_e32 v35, v35, v212
	v_add_f32_e32 v31, v31, v35
	s_waitcnt vmcnt(9)
	v_mul_f32_e32 v35, v201, v201
	v_mul_f32_e32 v212, v203, v203
	v_fmac_f32_e32 v35, v200, v200
	v_fmac_f32_e32 v212, v202, v202
	v_add_f32_e32 v35, v35, v212
	v_add_f32_e32 v31, v31, v35
	s_waitcnt vmcnt(8)
	v_mul_f32_e32 v35, v205, v205
	v_mul_f32_e32 v212, v207, v207
	v_fmac_f32_e32 v35, v204, v204
	v_fmac_f32_e32 v212, v206, v206
	v_add_f32_e32 v35, v35, v212
	v_add_f32_e32 v31, v31, v35
	s_waitcnt vmcnt(7)
	v_mul_f32_e32 v35, v209, v209
	v_mul_f32_e32 v212, v211, v211
	v_fmac_f32_e32 v35, v208, v208
	v_fmac_f32_e32 v212, v210, v210
	v_add_f32_e32 v32, v35, v212
	s_waitcnt vmcnt(6)
	v_mul_f32_e32 v35, v223, v223
	v_mul_f32_e32 v212, v225, v225
	v_fmac_f32_e32 v35, v222, v222
	v_fmac_f32_e32 v212, v224, v224
	v_add_f32_e32 v35, v35, v212
	v_add_f32_e32 v32, v32, v35
	s_waitcnt vmcnt(5)
	v_mul_f32_e32 v35, v227, v227
	v_mul_f32_e32 v212, v229, v229
	v_fmac_f32_e32 v35, v226, v226
	v_fmac_f32_e32 v212, v228, v228
	v_add_f32_e32 v35, v35, v212
	v_add_f32_e32 v32, v32, v35
	s_waitcnt vmcnt(4)
	v_mul_f32_e32 v35, v231, v231
	v_mul_f32_e32 v212, v233, v233
	v_fmac_f32_e32 v35, v230, v230
	v_fmac_f32_e32 v212, v232, v232
	v_add_f32_e32 v35, v35, v212
	v_add_f32_e32 v32, v32, v35
	s_waitcnt vmcnt(3)
	v_mul_f32_e32 v35, v239, v239
	v_mul_f32_e32 v212, v241, v241
	v_fmac_f32_e32 v35, v238, v238
	v_fmac_f32_e32 v212, v240, v240
	v_add_f32_e32 v35, v35, v212
	v_add_f32_e32 v32, v32, v35
	s_waitcnt vmcnt(2)
	v_mul_f32_e32 v35, v243, v243
	v_mul_f32_e32 v212, v245, v245
	v_fmac_f32_e32 v35, v242, v242
	v_fmac_f32_e32 v212, v244, v244
	v_add_f32_e32 v35, v35, v212
	v_add_f32_e32 v32, v32, v35
	s_waitcnt vmcnt(1)
	v_mul_f32_e32 v35, v247, v247
	v_mul_f32_e32 v212, v249, v249
	v_fmac_f32_e32 v35, v246, v246
	v_fmac_f32_e32 v212, v248, v248
	v_add_f32_e32 v35, v35, v212
	v_add_f32_e32 v32, v32, v35
	s_waitcnt vmcnt(0)
	v_mul_f32_e32 v35, v251, v251
	v_mul_f32_e32 v212, v253, v253
	v_fmac_f32_e32 v35, v250, v250
	v_fmac_f32_e32 v212, v252, v252
	v_add_f32_e32 v35, v35, v212
	v_add_f32_e32 v32, v32, v35
	s_nop 1
	v_mov_b32_dpp v36, v19 quad_perm:[1,0,3,2] row_mask:0xf bank_mask:0xf
	v_mov_b32_dpp v40, v28 quad_perm:[1,0,3,2] row_mask:0xf bank_mask:0xf
	v_mov_b32_dpp v44, v29 quad_perm:[1,0,3,2] row_mask:0xf bank_mask:0xf
	v_mov_b32_dpp v48, v30 quad_perm:[1,0,3,2] row_mask:0xf bank_mask:0xf
	v_mov_b32_dpp v52, v31 quad_perm:[1,0,3,2] row_mask:0xf bank_mask:0xf
	v_mov_b32_dpp v56, v32 quad_perm:[1,0,3,2] row_mask:0xf bank_mask:0xf
	v_add_f32_e32 v19, v19, v36
	v_add_f32_e32 v28, v28, v40
	v_add_f32_e32 v29, v29, v44
	v_add_f32_e32 v30, v30, v48
	v_add_f32_e32 v31, v31, v52
	v_add_f32_e32 v32, v32, v56
	s_nop 1
	v_mov_b32_dpp v36, v19 quad_perm:[2,3,0,1] row_mask:0xf bank_mask:0xf
	v_mov_b32_dpp v40, v28 quad_perm:[2,3,0,1] row_mask:0xf bank_mask:0xf
	v_mov_b32_dpp v44, v29 quad_perm:[2,3,0,1] row_mask:0xf bank_mask:0xf
	v_mov_b32_dpp v48, v30 quad_perm:[2,3,0,1] row_mask:0xf bank_mask:0xf
	v_mov_b32_dpp v52, v31 quad_perm:[2,3,0,1] row_mask:0xf bank_mask:0xf
	v_mov_b32_dpp v56, v32 quad_perm:[2,3,0,1] row_mask:0xf bank_mask:0xf
	v_add_f32_e32 v19, v19, v36
	v_add_f32_e32 v28, v28, v40
	v_add_f32_e32 v29, v29, v44
	v_add_f32_e32 v30, v30, v48
	v_add_f32_e32 v31, v31, v52
	v_add_f32_e32 v32, v32, v56
	s_nop 1
	v_mov_b32_dpp v36, v19 row_half_mirror row_mask:0xf bank_mask:0xf
	v_mov_b32_dpp v40, v28 row_half_mirror row_mask:0xf bank_mask:0xf
	v_mov_b32_dpp v44, v29 row_half_mirror row_mask:0xf bank_mask:0xf
	v_mov_b32_dpp v48, v30 row_half_mirror row_mask:0xf bank_mask:0xf
	v_mov_b32_dpp v52, v31 row_half_mirror row_mask:0xf bank_mask:0xf
	v_mov_b32_dpp v56, v32 row_half_mirror row_mask:0xf bank_mask:0xf
	v_add_f32_e32 v19, v19, v36
	v_add_f32_e32 v28, v28, v40
	v_add_f32_e32 v29, v29, v44
	v_add_f32_e32 v30, v30, v48
	v_add_f32_e32 v31, v31, v52
	v_add_f32_e32 v32, v32, v56
	s_nop 1
	v_mov_b32_dpp v36, v19 row_mirror row_mask:0xf bank_mask:0xf
	v_mov_b32_dpp v40, v28 row_mirror row_mask:0xf bank_mask:0xf
	v_mov_b32_dpp v44, v29 row_mirror row_mask:0xf bank_mask:0xf
	v_mov_b32_dpp v48, v30 row_mirror row_mask:0xf bank_mask:0xf
	v_mov_b32_dpp v52, v31 row_mirror row_mask:0xf bank_mask:0xf
	v_mov_b32_dpp v56, v32 row_mirror row_mask:0xf bank_mask:0xf
	v_add_f32_e32 v19, v19, v36
	v_add_f32_e32 v28, v28, v40
	v_add_f32_e32 v29, v29, v44
	v_add_f32_e32 v30, v30, v48
	v_add_f32_e32 v31, v31, v52
	v_add_f32_e32 v32, v32, v56
	v_mov_b32_e32 v36, v19
	v_mov_b32_e32 v40, v28
	v_mov_b32_e32 v44, v29
	v_mov_b32_e32 v48, v30
	v_mov_b32_e32 v52, v31
	v_mov_b32_e32 v56, v32
	s_nop 1
	v_permlane16_swap_b32_e32 v36, v19
	v_permlane16_swap_b32_e32 v40, v28
	v_permlane16_swap_b32_e32 v44, v29
	v_permlane16_swap_b32_e32 v48, v30
	v_permlane16_swap_b32_e32 v52, v31
	v_permlane16_swap_b32_e32 v56, v32
	v_add_f32_e32 v19, v19, v36
	v_add_f32_e32 v28, v28, v40
	v_add_f32_e32 v29, v29, v44
	v_add_f32_e32 v30, v30, v48
	v_add_f32_e32 v31, v31, v52
	v_add_f32_e32 v32, v32, v56
	v_mov_b32_e32 v36, v19
	v_mov_b32_e32 v40, v28
	v_mov_b32_e32 v44, v29
	v_mov_b32_e32 v48, v30
	v_mov_b32_e32 v52, v31
	v_mov_b32_e32 v56, v32
	s_nop 1
	v_permlane32_swap_b32_e32 v36, v19
	v_permlane32_swap_b32_e32 v40, v28
	v_permlane32_swap_b32_e32 v44, v29
	v_permlane32_swap_b32_e32 v48, v30
	v_permlane32_swap_b32_e32 v52, v31
	v_permlane32_swap_b32_e32 v56, v32
	v_add_f32_e32 v19, v19, v36
	v_add_f32_e32 v28, v28, v40
	v_add_f32_e32 v29, v29, v44
	v_add_f32_e32 v30, v30, v48
	v_add_f32_e32 v31, v31, v52
	v_add_f32_e32 v32, v32, v56
	s_and_saveexec_b64 s[6:7], s[0:1]
	s_cbranch_execz .Lcal_w
	v_mov_b32_e32 v35, s18
	ds_write_b32 v35, v19
	ds_write_b32 v35, v28 offset:32
	ds_write_b32 v35, v29 offset:64
	ds_write_b32 v35, v30 offset:96
	ds_write_b32 v35, v31 offset:128
	ds_write_b32 v35, v32 offset:160
.Lcal_w:
	s_or_b64 exec, exec, s[6:7]
	s_waitcnt lgkmcnt(0)
	s_barrier
	v_cmp_gt_u32_e64 s[6:7], 6, v234
	s_and_saveexec_b64 s[12:13], s[6:7]
	s_cbranch_execz .Lcal_s
	v_lshlrev_b32_e32 v212, 5, v234
	ds_read_b128 v[36:39], v212
	ds_read_b128 v[40:43], v212 offset:16
	s_waitcnt lgkmcnt(1)
	v_add_f32_e32 v35, 0, v36
	v_add_f32_e32 v35, v35, v37
	v_add_f32_e32 v35, v35, v38
	v_add_f32_e32 v35, v35, v39
	s_waitcnt lgkmcnt(0)
	v_add_f32_e32 v35, v35, v40
	v_add_f32_e32 v35, v35, v41
	v_add_f32_e32 v35, v35, v42
	v_add_f32_e32 v35, v35, v43
	v_mul_f32_e32 v35, 0x38800000, v35
	v_mul_f32_e32 v36, 0x4f800000, v35
	v_cmp_gt_f32_e32 vcc, s19, v35
	s_nop 1
	v_cndmask_b32_e32 v35, v35, v36, vcc
	v_sqrt_f32_e32 v36, v35
	s_nop 0
	v_add_u32_e32 v37, -1, v36
	v_add_u32_e32 v38, 1, v36
	v_fma_f32 v39, -v37, v36, v35
	v_fma_f32 v40, -v38, v36, v35
	v_cmp_ge_f32_e64 s[6:7], 0, v39
	s_nop 1
	v_cndmask_b32_e64 v36, v36, v37, s[6:7]
	v_cmp_lt_f32_e64 s[6:7], 0, v40
	s_nop 1
	v_cndmask_b32_e64 v36, v36, v38, s[6:7]
	v_mul_f32_e32 v37, 0x37800000, v36
	v_cndmask_b32_e32 v36, v36, v37, vcc
	v_cmp_class_f32_e32 vcc, v35, v34
	s_nop 1
	v_cndmask_b32_e32 v35, v36, v35, vcc
	v_max_f32_e32 v35, 0xda24260, v35
	v_mul_f32_e32 v35, 0x40900000, v35
	v_div_scale_f32 v36, s[6:7], v35, v35, s20
	v_rcp_f32_e32 v37, v36
	v_div_scale_f32 v38, vcc, s20, v35, s20
	v_fma_f32 v39, -v36, v37, 1.0
	v_fmac_f32_e32 v37, v39, v37
	v_mul_f32_e32 v39, v38, v37
	v_fma_f32 v40, -v36, v39, v38
	v_fmac_f32_e32 v39, v40, v37
	v_fma_f32 v36, -v36, v39, v38
	v_div_fmas_f32 v36, v36, v37, v39
	v_div_fixup_f32 v35, v36, v35, s20
	v_mov_b32_e32 v36, s17
	v_lshl_add_u32 v36, v234, 2, v36
	s_andn2_b64 vcc, exec, s[8:9]
	ds_write_b32 v36, v35
	s_cbranch_vccnz .Lcal_s
	v_lshlrev_b32_e32 v36, 2, v234
	global_store_dword v36, v35, s[10:11]
.Lcal_s:
	s_or_b64 exec, exec, s[12:13]
	s_mov_b32 s16, 6
	s_add_i32 s17, s17, 24
	s_add_u32 s10, s10, 24
	s_addc_u32 s11, s11, 0
	s_mov_b64 s[6:7], s[66:67]
	s_mov_b64 s[12:13], 0x1c00000
	s_mov_b64 s[14:15], 0
	v_readlane_b32 s36, v254, 24
	v_readlane_b32 s37, v254, 25
	v_readlane_b32 s38, v254, 26
	v_readlane_b32 s39, v254, 27
	v_readlane_b32 s40, v254, 28
	v_readlane_b32 s41, v254, 29
	v_readlane_b32 s42, v254, 30
	v_readlane_b32 s43, v254, 31
	v_readlane_b32 s44, v254, 32
	v_readlane_b32 s45, v254, 33
	v_readlane_b32 s46, v254, 34
	v_readlane_b32 s47, v254, 35
	v_readlane_b32 s48, v254, 36
	v_readlane_b32 s49, v254, 37
	v_readlane_b32 s50, v254, 38
	v_readlane_b32 s51, v254, 39
	s_waitcnt lgkmcnt(0)
	s_barrier

.LBB0_2674:
	ds_read_b64_tr_b16 v[134:135], v204 offset:0
	ds_read_b64_tr_b16 v[136:137], v204 offset:0x800
	ds_read_b64_tr_b16 v[138:139], v204 offset:0x1000
	ds_read_b64_tr_b16 v[140:141], v204 offset:0x1800
	ds_read_b64_tr_b16 v[142:143], v204 offset:0x2000
	ds_read_b64_tr_b16 v[144:145], v204 offset:0x2800
	ds_read_b64_tr_b16 v[146:147], v204 offset:0x3000
	ds_read_b64_tr_b16 v[148:149], v204 offset:0x3800
	s_nop 0
	s_waitcnt lgkmcnt(6)
	v_mfma_f32_32x32x16_bf16 v[82:97], v[20:23], v[134:137], v[82:97]
	ds_read_b64_tr_b16 v[134:135], v204 offset:0x200
	ds_read_b64_tr_b16 v[136:137], v204 offset:0xa00
	s_waitcnt lgkmcnt(6)
	v_mfma_f32_32x32x16_bf16 v[82:97], v[24:27], v[138:141], v[82:97]
	ds_read_b64_tr_b16 v[138:139], v204 offset:0x1200
	ds_read_b64_tr_b16 v[140:141], v204 offset:0x1a00
	s_waitcnt lgkmcnt(6)
	v_mfma_f32_32x32x16_bf16 v[82:97], v[28:31], v[142:145], v[82:97]
	ds_read_b64_tr_b16 v[142:143], v204 offset:0x2200
	ds_read_b64_tr_b16 v[144:145], v204 offset:0x2a00
	s_waitcnt lgkmcnt(6)
	v_mfma_f32_32x32x16_bf16 v[82:97], v[130:133], v[146:149], v[82:97]
	ds_read_b64_tr_b16 v[146:147], v204 offset:0x3200
	ds_read_b64_tr_b16 v[148:149], v204 offset:0x3a00
	s_waitcnt lgkmcnt(6)
	v_mfma_f32_32x32x16_bf16 v[66:81], v[20:23], v[134:137], v[66:81]
	ds_read_b64_tr_b16 v[134:135], v204 offset:0x400
	ds_read_b64_tr_b16 v[136:137], v204 offset:0xc00
	s_waitcnt lgkmcnt(6)
	v_mfma_f32_32x32x16_bf16 v[66:81], v[24:27], v[138:141], v[66:81]
	ds_read_b64_tr_b16 v[138:139], v204 offset:0x1400
	ds_read_b64_tr_b16 v[140:141], v204 offset:0x1c00
	s_waitcnt lgkmcnt(6)
	v_mfma_f32_32x32x16_bf16 v[66:81], v[28:31], v[142:145], v[66:81]
	ds_read_b64_tr_b16 v[142:143], v204 offset:0x2400
	ds_read_b64_tr_b16 v[144:145], v204 offset:0x2c00
	s_waitcnt lgkmcnt(6)
	v_mfma_f32_32x32x16_bf16 v[66:81], v[130:133], v[146:149], v[66:81]
	ds_read_b64_tr_b16 v[146:147], v204 offset:0x3400
	ds_read_b64_tr_b16 v[148:149], v204 offset:0x3c00
	s_waitcnt lgkmcnt(6)
	v_mfma_f32_32x32x16_bf16 v[50:65], v[20:23], v[134:137], v[50:65]
	ds_read_b64_tr_b16 v[134:135], v204 offset:0x600
	ds_read_b64_tr_b16 v[136:137], v204 offset:0xe00
	s_waitcnt lgkmcnt(6)
	v_mfma_f32_32x32x16_bf16 v[50:65], v[24:27], v[138:141], v[50:65]
	ds_read_b64_tr_b16 v[138:139], v204 offset:0x1600
	ds_read_b64_tr_b16 v[140:141], v204 offset:0x1e00
	s_waitcnt lgkmcnt(6)
	v_mfma_f32_32x32x16_bf16 v[50:65], v[28:31], v[142:145], v[50:65]
	ds_read_b64_tr_b16 v[142:143], v204 offset:0x2600
	ds_read_b64_tr_b16 v[144:145], v204 offset:0x2e00
	s_waitcnt lgkmcnt(6)
	v_mfma_f32_32x32x16_bf16 v[50:65], v[130:133], v[146:149], v[50:65]
	ds_read_b64_tr_b16 v[146:147], v204 offset:0x3600
	ds_read_b64_tr_b16 v[148:149], v204 offset:0x3e00
	s_waitcnt lgkmcnt(6)
	v_mfma_f32_32x32x16_bf16 v[34:49], v[20:23], v[134:137], v[34:49]
	s_waitcnt lgkmcnt(4)
	v_mfma_f32_32x32x16_bf16 v[34:49], v[24:27], v[138:141], v[34:49]
	s_waitcnt lgkmcnt(2)
	v_mfma_f32_32x32x16_bf16 v[34:49], v[28:31], v[142:145], v[34:49]
	s_waitcnt lgkmcnt(0)
	v_mfma_f32_32x32x16_bf16 v[34:49], v[130:133], v[146:149], v[34:49]
	s_and_b64 vcc, exec, s[10:11]
	s_cbranch_vccnz .LBB0_2679

.LBB0_2703:
	s_cmp_le_i32 s95, s84
	s_cselect_b64 s[12:13], -1, 0
	s_lshr_b32 s3, s82, s91
	v_cndmask_b32_e64 v2, 0, 1, s[12:13]
	v_mov_b32_e32 v33, s3
	v_cndmask_b32_e64 v2, v33, v2, s[8:9]
	v_and_b32_e32 v2, 1, v2
	v_cmp_eq_u32_e32 vcc, 0, v2
	s_cbranch_vccnz .LBB0_2705
	ds_read_b64_tr_b16 v[134:135], v204 offset:0x4000
	ds_read_b64_tr_b16 v[136:137], v204 offset:0x4800
	ds_read_b64_tr_b16 v[138:139], v204 offset:0x5000
	ds_read_b64_tr_b16 v[140:141], v204 offset:0x5800
	ds_read_b64_tr_b16 v[142:143], v204 offset:0x6000
	ds_read_b64_tr_b16 v[144:145], v204 offset:0x6800
	ds_read_b64_tr_b16 v[146:147], v204 offset:0x7000
	ds_read_b64_tr_b16 v[148:149], v204 offset:0x7800
	s_nop 0
	s_waitcnt lgkmcnt(6)
	v_mfma_f32_32x32x16_bf16 v[82:97], v[20:23], v[134:137], v[82:97]
	ds_read_b64_tr_b16 v[134:135], v204 offset:0x4200
	ds_read_b64_tr_b16 v[136:137], v204 offset:0x4a00
	s_waitcnt lgkmcnt(6)
	v_mfma_f32_32x32x16_bf16 v[82:97], v[24:27], v[138:141], v[82:97]
	ds_read_b64_tr_b16 v[138:139], v204 offset:0x5200
	ds_read_b64_tr_b16 v[140:141], v204 offset:0x5a00
	s_waitcnt lgkmcnt(6)
	v_mfma_f32_32x32x16_bf16 v[82:97], v[28:31], v[142:145], v[82:97]
	ds_read_b64_tr_b16 v[142:143], v204 offset:0x6200
	ds_read_b64_tr_b16 v[144:145], v204 offset:0x6a00
	s_waitcnt lgkmcnt(6)
	v_mfma_f32_32x32x16_bf16 v[82:97], v[130:133], v[146:149], v[82:97]
	ds_read_b64_tr_b16 v[146:147], v204 offset:0x7200
	ds_read_b64_tr_b16 v[148:149], v204 offset:0x7a00
	s_waitcnt lgkmcnt(6)
	v_mfma_f32_32x32x16_bf16 v[66:81], v[20:23], v[134:137], v[66:81]
	ds_read_b64_tr_b16 v[134:135], v204 offset:0x4400
	ds_read_b64_tr_b16 v[136:137], v204 offset:0x4c00
	s_waitcnt lgkmcnt(6)
	v_mfma_f32_32x32x16_bf16 v[66:81], v[24:27], v[138:141], v[66:81]
	ds_read_b64_tr_b16 v[138:139], v204 offset:0x5400
	ds_read_b64_tr_b16 v[140:141], v204 offset:0x5c00
	s_waitcnt lgkmcnt(6)
	v_mfma_f32_32x32x16_bf16 v[66:81], v[28:31], v[142:145], v[66:81]
	ds_read_b64_tr_b16 v[142:143], v204 offset:0x6400
	ds_read_b64_tr_b16 v[144:145], v204 offset:0x6c00
	s_waitcnt lgkmcnt(6)
	v_mfma_f32_32x32x16_bf16 v[66:81], v[130:133], v[146:149], v[66:81]
	ds_read_b64_tr_b16 v[146:147], v204 offset:0x7400
	ds_read_b64_tr_b16 v[148:149], v204 offset:0x7c00
	s_waitcnt lgkmcnt(6)
	v_mfma_f32_32x32x16_bf16 v[50:65], v[20:23], v[134:137], v[50:65]
	ds_read_b64_tr_b16 v[134:135], v204 offset:0x4600
	ds_read_b64_tr_b16 v[136:137], v204 offset:0x4e00
	s_waitcnt lgkmcnt(6)
	v_mfma_f32_32x32x16_bf16 v[50:65], v[24:27], v[138:141], v[50:65]
	ds_read_b64_tr_b16 v[138:139], v204 offset:0x5600
	ds_read_b64_tr_b16 v[140:141], v204 offset:0x5e00
	s_waitcnt lgkmcnt(6)
	v_mfma_f32_32x32x16_bf16 v[50:65], v[28:31], v[142:145], v[50:65]
	ds_read_b64_tr_b16 v[142:143], v204 offset:0x6600
	ds_read_b64_tr_b16 v[144:145], v204 offset:0x6e00
	s_waitcnt lgkmcnt(6)
	v_mfma_f32_32x32x16_bf16 v[50:65], v[130:133], v[146:149], v[50:65]
	ds_read_b64_tr_b16 v[146:147], v204 offset:0x7600
	ds_read_b64_tr_b16 v[148:149], v204 offset:0x7e00
	s_waitcnt lgkmcnt(6)
	v_mfma_f32_32x32x16_bf16 v[34:49], v[20:23], v[134:137], v[34:49]
	s_waitcnt lgkmcnt(4)
	v_mfma_f32_32x32x16_bf16 v[34:49], v[24:27], v[138:141], v[34:49]
	s_waitcnt lgkmcnt(2)
	v_mfma_f32_32x32x16_bf16 v[34:49], v[28:31], v[142:145], v[34:49]
	s_waitcnt lgkmcnt(0)
	v_mfma_f32_32x32x16_bf16 v[34:49], v[130:133], v[146:149], v[34:49]

.LBB0_2735:
	ds_read_b64_tr_b16 v[138:139], v204 offset:0
	ds_read_b64_tr_b16 v[140:141], v204 offset:0x800
	ds_read_b64_tr_b16 v[142:143], v204 offset:0x1000
	ds_read_b64_tr_b16 v[144:145], v204 offset:0x1800
	ds_read_b64_tr_b16 v[146:147], v204 offset:0x2000
	ds_read_b64_tr_b16 v[148:149], v204 offset:0x2800
	ds_read_b64_tr_b16 v[150:151], v204 offset:0x3000
	ds_read_b64_tr_b16 v[152:153], v204 offset:0x3800
	s_nop 0
	s_waitcnt lgkmcnt(6)
	v_mfma_f32_32x32x16_bf16 v[82:97], v[24:27], v[138:141], v[82:97]
	ds_read_b64_tr_b16 v[138:139], v204 offset:0x200
	ds_read_b64_tr_b16 v[140:141], v204 offset:0xa00
	s_waitcnt lgkmcnt(6)
	v_mfma_f32_32x32x16_bf16 v[82:97], v[28:31], v[142:145], v[82:97]
	ds_read_b64_tr_b16 v[142:143], v204 offset:0x1200
	ds_read_b64_tr_b16 v[144:145], v204 offset:0x1a00
	s_waitcnt lgkmcnt(6)
	v_mfma_f32_32x32x16_bf16 v[82:97], v[130:133], v[146:149], v[82:97]
	ds_read_b64_tr_b16 v[146:147], v204 offset:0x2200
	ds_read_b64_tr_b16 v[148:149], v204 offset:0x2a00
	s_waitcnt lgkmcnt(6)
	v_mfma_f32_32x32x16_bf16 v[82:97], v[134:137], v[150:153], v[82:97]
	ds_read_b64_tr_b16 v[150:151], v204 offset:0x3200
	ds_read_b64_tr_b16 v[152:153], v204 offset:0x3a00
	s_waitcnt lgkmcnt(6)
	v_mfma_f32_32x32x16_bf16 v[66:81], v[24:27], v[138:141], v[66:81]
	ds_read_b64_tr_b16 v[138:139], v204 offset:0x400
	ds_read_b64_tr_b16 v[140:141], v204 offset:0xc00
	s_waitcnt lgkmcnt(6)
	v_mfma_f32_32x32x16_bf16 v[66:81], v[28:31], v[142:145], v[66:81]
	ds_read_b64_tr_b16 v[142:143], v204 offset:0x1400
	ds_read_b64_tr_b16 v[144:145], v204 offset:0x1c00
	s_waitcnt lgkmcnt(6)
	v_mfma_f32_32x32x16_bf16 v[66:81], v[130:133], v[146:149], v[66:81]
	ds_read_b64_tr_b16 v[146:147], v204 offset:0x2400
	ds_read_b64_tr_b16 v[148:149], v204 offset:0x2c00
	s_waitcnt lgkmcnt(6)
	v_mfma_f32_32x32x16_bf16 v[66:81], v[134:137], v[150:153], v[66:81]
	ds_read_b64_tr_b16 v[150:151], v204 offset:0x3400
	ds_read_b64_tr_b16 v[152:153], v204 offset:0x3c00
	s_waitcnt lgkmcnt(6)
	v_mfma_f32_32x32x16_bf16 v[50:65], v[24:27], v[138:141], v[50:65]
	ds_read_b64_tr_b16 v[138:139], v204 offset:0x600
	ds_read_b64_tr_b16 v[140:141], v204 offset:0xe00
	s_waitcnt lgkmcnt(6)
	v_mfma_f32_32x32x16_bf16 v[50:65], v[28:31], v[142:145], v[50:65]
	ds_read_b64_tr_b16 v[142:143], v204 offset:0x1600
	ds_read_b64_tr_b16 v[144:145], v204 offset:0x1e00
	s_waitcnt lgkmcnt(6)
	v_mfma_f32_32x32x16_bf16 v[50:65], v[130:133], v[146:149], v[50:65]
	ds_read_b64_tr_b16 v[146:147], v204 offset:0x2600
	ds_read_b64_tr_b16 v[148:149], v204 offset:0x2e00
	s_waitcnt lgkmcnt(6)
	v_mfma_f32_32x32x16_bf16 v[50:65], v[134:137], v[150:153], v[50:65]
	ds_read_b64_tr_b16 v[150:151], v204 offset:0x3600
	ds_read_b64_tr_b16 v[152:153], v204 offset:0x3e00
	s_waitcnt lgkmcnt(6)
	v_mfma_f32_32x32x16_bf16 v[34:49], v[24:27], v[138:141], v[34:49]
	s_waitcnt lgkmcnt(4)
	v_mfma_f32_32x32x16_bf16 v[34:49], v[28:31], v[142:145], v[34:49]
	s_waitcnt lgkmcnt(2)
	v_mfma_f32_32x32x16_bf16 v[34:49], v[130:133], v[146:149], v[34:49]
	s_waitcnt lgkmcnt(0)
	v_mfma_f32_32x32x16_bf16 v[34:49], v[134:137], v[150:153], v[34:49]
	s_and_b64 vcc, exec, s[70:71]
	s_cbranch_vccnz .LBB0_2887

.LBB0_2753:
	ds_read_b64_tr_b16 v[106:107], v204 offset:0x4000
	ds_read_b64_tr_b16 v[108:109], v204 offset:0x4800
	ds_read_b64_tr_b16 v[110:111], v204 offset:0x5000
	ds_read_b64_tr_b16 v[112:113], v204 offset:0x5800
	ds_read_b64_tr_b16 v[114:115], v204 offset:0x6000
	ds_read_b64_tr_b16 v[116:117], v204 offset:0x6800
	ds_read_b64_tr_b16 v[118:119], v204 offset:0x7000
	ds_read_b64_tr_b16 v[120:121], v204 offset:0x7800
	s_nop 0
	s_waitcnt lgkmcnt(6)
	v_mfma_f32_32x32x16_bf16 v[82:97], v[24:27], v[106:109], v[82:97]
	ds_read_b64_tr_b16 v[106:107], v204 offset:0x4200
	ds_read_b64_tr_b16 v[108:109], v204 offset:0x4a00
	s_waitcnt lgkmcnt(6)
	v_mfma_f32_32x32x16_bf16 v[82:97], v[28:31], v[110:113], v[82:97]
	ds_read_b64_tr_b16 v[110:111], v204 offset:0x5200
	ds_read_b64_tr_b16 v[112:113], v204 offset:0x5a00
	s_waitcnt lgkmcnt(6)
	v_mfma_f32_32x32x16_bf16 v[82:97], v[98:101], v[114:117], v[82:97]
	ds_read_b64_tr_b16 v[114:115], v204 offset:0x6200
	ds_read_b64_tr_b16 v[116:117], v204 offset:0x6a00
	ds_read_b64_tr_b16 v[122:123], v204 offset:0x7200
	ds_read_b64_tr_b16 v[124:125], v204 offset:0x7a00
	s_waitcnt lgkmcnt(8)
	v_mfma_f32_32x32x16_bf16 v[82:97], v[102:105], v[118:121], v[82:97]
	s_waitcnt lgkmcnt(6)
	v_mfma_f32_32x32x16_bf16 v[66:81], v[24:27], v[106:109], v[66:81]
	ds_read_b64_tr_b16 v[106:107], v204 offset:0x4400
	ds_read_b64_tr_b16 v[108:109], v204 offset:0x4c00
	s_waitcnt lgkmcnt(6)
	v_mfma_f32_32x32x16_bf16 v[66:81], v[28:31], v[110:113], v[66:81]
	ds_read_b64_tr_b16 v[110:111], v204 offset:0x5400
	ds_read_b64_tr_b16 v[112:113], v204 offset:0x5c00
	s_waitcnt lgkmcnt(6)
	v_mfma_f32_32x32x16_bf16 v[66:81], v[98:101], v[114:117], v[66:81]
	ds_read_b64_tr_b16 v[114:115], v204 offset:0x6400
	ds_read_b64_tr_b16 v[116:117], v204 offset:0x6c00
	ds_read_b64_tr_b16 v[118:119], v204 offset:0x7400
	ds_read_b64_tr_b16 v[120:121], v204 offset:0x7c00
	s_waitcnt lgkmcnt(8)
	v_mfma_f32_32x32x16_bf16 v[66:81], v[102:105], v[122:125], v[66:81]
	s_waitcnt lgkmcnt(6)
	v_mfma_f32_32x32x16_bf16 v[50:65], v[24:27], v[106:109], v[50:65]
	ds_read_b64_tr_b16 v[106:107], v204 offset:0x4600
	ds_read_b64_tr_b16 v[108:109], v204 offset:0x4e00
	s_waitcnt lgkmcnt(6)
	v_mfma_f32_32x32x16_bf16 v[50:65], v[28:31], v[110:113], v[50:65]
	ds_read_b64_tr_b16 v[110:111], v204 offset:0x5600
	ds_read_b64_tr_b16 v[112:113], v204 offset:0x5e00
	s_waitcnt lgkmcnt(6)
	v_mfma_f32_32x32x16_bf16 v[50:65], v[98:101], v[114:117], v[50:65]
	ds_read_b64_tr_b16 v[114:115], v204 offset:0x6600
	ds_read_b64_tr_b16 v[116:117], v204 offset:0x6e00
	ds_read_b64_tr_b16 v[122:123], v204 offset:0x7600
	ds_read_b64_tr_b16 v[124:125], v204 offset:0x7e00
	s_waitcnt lgkmcnt(8)
	v_mfma_f32_32x32x16_bf16 v[50:65], v[102:105], v[118:121], v[50:65]
	s_waitcnt lgkmcnt(6)
	v_mfma_f32_32x32x16_bf16 v[34:49], v[24:27], v[106:109], v[34:49]
	s_waitcnt lgkmcnt(4)
	v_mfma_f32_32x32x16_bf16 v[34:49], v[28:31], v[110:113], v[34:49]
	s_waitcnt lgkmcnt(2)
	v_mfma_f32_32x32x16_bf16 v[34:49], v[98:101], v[114:117], v[34:49]
	s_waitcnt lgkmcnt(0)
	v_mfma_f32_32x32x16_bf16 v[34:49], v[102:105], v[122:125], v[34:49]

.LBB0_3241:
	ds_read_b64_tr_b16 v[134:135], v203 offset:0
	ds_read_b64_tr_b16 v[136:137], v203 offset:0x800
	ds_read_b64_tr_b16 v[138:139], v203 offset:0x1000
	ds_read_b64_tr_b16 v[140:141], v203 offset:0x1800
	ds_read_b64_tr_b16 v[142:143], v203 offset:0x2000
	ds_read_b64_tr_b16 v[144:145], v203 offset:0x2800
	ds_read_b64_tr_b16 v[146:147], v203 offset:0x3000
	ds_read_b64_tr_b16 v[148:149], v203 offset:0x3800
	s_nop 0
	s_waitcnt lgkmcnt(6)
	v_mfma_f32_32x32x16_bf16 v[82:97], v[20:23], v[134:137], v[82:97]
	ds_read_b64_tr_b16 v[134:135], v203 offset:0x200
	ds_read_b64_tr_b16 v[136:137], v203 offset:0xa00
	s_waitcnt lgkmcnt(6)
	v_mfma_f32_32x32x16_bf16 v[82:97], v[24:27], v[138:141], v[82:97]
	ds_read_b64_tr_b16 v[138:139], v203 offset:0x1200
	ds_read_b64_tr_b16 v[140:141], v203 offset:0x1a00
	s_waitcnt lgkmcnt(6)
	v_mfma_f32_32x32x16_bf16 v[82:97], v[28:31], v[142:145], v[82:97]
	ds_read_b64_tr_b16 v[142:143], v203 offset:0x2200
	ds_read_b64_tr_b16 v[144:145], v203 offset:0x2a00
	ds_read_b64_tr_b16 v[150:151], v203 offset:0x3200
	ds_read_b64_tr_b16 v[152:153], v203 offset:0x3a00
	s_waitcnt lgkmcnt(8)
	v_mfma_f32_32x32x16_bf16 v[82:97], v[130:133], v[146:149], v[82:97]
	s_waitcnt lgkmcnt(6)
	v_mfma_f32_32x32x16_bf16 v[66:81], v[20:23], v[134:137], v[66:81]
	ds_read_b64_tr_b16 v[134:135], v203 offset:0x400
	ds_read_b64_tr_b16 v[136:137], v203 offset:0xc00
	s_waitcnt lgkmcnt(6)
	v_mfma_f32_32x32x16_bf16 v[66:81], v[24:27], v[138:141], v[66:81]
	ds_read_b64_tr_b16 v[138:139], v203 offset:0x1400
	ds_read_b64_tr_b16 v[140:141], v203 offset:0x1c00
	s_waitcnt lgkmcnt(6)
	v_mfma_f32_32x32x16_bf16 v[66:81], v[28:31], v[142:145], v[66:81]
	ds_read_b64_tr_b16 v[142:143], v203 offset:0x2400
	ds_read_b64_tr_b16 v[144:145], v203 offset:0x2c00
	ds_read_b64_tr_b16 v[146:147], v203 offset:0x3400
	ds_read_b64_tr_b16 v[148:149], v203 offset:0x3c00
	s_waitcnt lgkmcnt(8)
	v_mfma_f32_32x32x16_bf16 v[66:81], v[130:133], v[150:153], v[66:81]
	s_waitcnt lgkmcnt(6)
	v_mfma_f32_32x32x16_bf16 v[50:65], v[20:23], v[134:137], v[50:65]
	ds_read_b64_tr_b16 v[134:135], v203 offset:0x600
	ds_read_b64_tr_b16 v[136:137], v203 offset:0xe00
	s_waitcnt lgkmcnt(6)
	v_mfma_f32_32x32x16_bf16 v[50:65], v[24:27], v[138:141], v[50:65]
	ds_read_b64_tr_b16 v[138:139], v203 offset:0x1600
	ds_read_b64_tr_b16 v[140:141], v203 offset:0x1e00
	s_waitcnt lgkmcnt(6)
	v_mfma_f32_32x32x16_bf16 v[50:65], v[28:31], v[142:145], v[50:65]
	ds_read_b64_tr_b16 v[142:143], v203 offset:0x2600
	ds_read_b64_tr_b16 v[144:145], v203 offset:0x2e00
	ds_read_b64_tr_b16 v[150:151], v203 offset:0x3600
	ds_read_b64_tr_b16 v[152:153], v203 offset:0x3e00
	s_waitcnt lgkmcnt(8)
	v_mfma_f32_32x32x16_bf16 v[50:65], v[130:133], v[146:149], v[50:65]
	s_waitcnt lgkmcnt(6)
	v_mfma_f32_32x32x16_bf16 v[34:49], v[20:23], v[134:137], v[34:49]
	s_waitcnt lgkmcnt(4)
	v_mfma_f32_32x32x16_bf16 v[34:49], v[24:27], v[138:141], v[34:49]
	s_waitcnt lgkmcnt(2)
	v_mfma_f32_32x32x16_bf16 v[34:49], v[28:31], v[142:145], v[34:49]
	s_waitcnt lgkmcnt(0)
	v_mfma_f32_32x32x16_bf16 v[34:49], v[130:133], v[150:153], v[34:49]
	s_and_b64 vcc, exec, s[10:11]
	s_cbranch_vccnz .LBB0_3246

.LBB0_3270:
	s_cmp_le_i32 s95, s85
	s_cselect_b64 s[12:13], -1, 0
	s_lshr_b32 s3, s83, s3
	v_cndmask_b32_e64 v2, 0, 1, s[12:13]
	v_mov_b32_e32 v33, s3
	v_cndmask_b32_e64 v2, v33, v2, s[8:9]
	v_and_b32_e32 v2, 1, v2
	v_cmp_eq_u32_e32 vcc, 0, v2
	s_cbranch_vccnz .LBB0_3272
	ds_read_b64_tr_b16 v[134:135], v203 offset:0x4000
	ds_read_b64_tr_b16 v[136:137], v203 offset:0x4800
	ds_read_b64_tr_b16 v[138:139], v203 offset:0x5000
	ds_read_b64_tr_b16 v[140:141], v203 offset:0x5800
	ds_read_b64_tr_b16 v[142:143], v203 offset:0x6000
	ds_read_b64_tr_b16 v[144:145], v203 offset:0x6800
	ds_read_b64_tr_b16 v[146:147], v203 offset:0x7000
	ds_read_b64_tr_b16 v[148:149], v203 offset:0x7800
	s_nop 0
	s_waitcnt lgkmcnt(6)
	v_mfma_f32_32x32x16_bf16 v[82:97], v[20:23], v[134:137], v[82:97]
	ds_read_b64_tr_b16 v[134:135], v203 offset:0x4200
	ds_read_b64_tr_b16 v[136:137], v203 offset:0x4a00
	s_waitcnt lgkmcnt(6)
	v_mfma_f32_32x32x16_bf16 v[82:97], v[24:27], v[138:141], v[82:97]
	ds_read_b64_tr_b16 v[138:139], v203 offset:0x5200
	ds_read_b64_tr_b16 v[140:141], v203 offset:0x5a00
	s_waitcnt lgkmcnt(6)
	v_mfma_f32_32x32x16_bf16 v[82:97], v[28:31], v[142:145], v[82:97]
	ds_read_b64_tr_b16 v[142:143], v203 offset:0x6200
	ds_read_b64_tr_b16 v[144:145], v203 offset:0x6a00
	ds_read_b64_tr_b16 v[150:151], v203 offset:0x7200
	ds_read_b64_tr_b16 v[152:153], v203 offset:0x7a00
	s_waitcnt lgkmcnt(8)
	v_mfma_f32_32x32x16_bf16 v[82:97], v[130:133], v[146:149], v[82:97]
	s_waitcnt lgkmcnt(6)
	v_mfma_f32_32x32x16_bf16 v[66:81], v[20:23], v[134:137], v[66:81]
	ds_read_b64_tr_b16 v[134:135], v203 offset:0x4400
	ds_read_b64_tr_b16 v[136:137], v203 offset:0x4c00
	s_waitcnt lgkmcnt(6)
	v_mfma_f32_32x32x16_bf16 v[66:81], v[24:27], v[138:141], v[66:81]
	ds_read_b64_tr_b16 v[138:139], v203 offset:0x5400
	ds_read_b64_tr_b16 v[140:141], v203 offset:0x5c00
	s_waitcnt lgkmcnt(6)
	v_mfma_f32_32x32x16_bf16 v[66:81], v[28:31], v[142:145], v[66:81]
	ds_read_b64_tr_b16 v[142:143], v203 offset:0x6400
	ds_read_b64_tr_b16 v[144:145], v203 offset:0x6c00
	ds_read_b64_tr_b16 v[146:147], v203 offset:0x7400
	ds_read_b64_tr_b16 v[148:149], v203 offset:0x7c00
	s_waitcnt lgkmcnt(8)
	v_mfma_f32_32x32x16_bf16 v[66:81], v[130:133], v[150:153], v[66:81]
	s_waitcnt lgkmcnt(6)
	v_mfma_f32_32x32x16_bf16 v[50:65], v[20:23], v[134:137], v[50:65]
	ds_read_b64_tr_b16 v[134:135], v203 offset:0x4600
	ds_read_b64_tr_b16 v[136:137], v203 offset:0x4e00
	s_waitcnt lgkmcnt(6)
	v_mfma_f32_32x32x16_bf16 v[50:65], v[24:27], v[138:141], v[50:65]
	ds_read_b64_tr_b16 v[138:139], v203 offset:0x5600
	ds_read_b64_tr_b16 v[140:141], v203 offset:0x5e00
	s_waitcnt lgkmcnt(6)
	v_mfma_f32_32x32x16_bf16 v[50:65], v[28:31], v[142:145], v[50:65]
	ds_read_b64_tr_b16 v[142:143], v203 offset:0x6600
	ds_read_b64_tr_b16 v[144:145], v203 offset:0x6e00
	ds_read_b64_tr_b16 v[150:151], v203 offset:0x7600
	ds_read_b64_tr_b16 v[152:153], v203 offset:0x7e00
	s_waitcnt lgkmcnt(8)
	v_mfma_f32_32x32x16_bf16 v[50:65], v[130:133], v[146:149], v[50:65]
	s_waitcnt lgkmcnt(6)
	v_mfma_f32_32x32x16_bf16 v[34:49], v[20:23], v[134:137], v[34:49]
	s_waitcnt lgkmcnt(4)
	v_mfma_f32_32x32x16_bf16 v[34:49], v[24:27], v[138:141], v[34:49]
	s_waitcnt lgkmcnt(2)
	v_mfma_f32_32x32x16_bf16 v[34:49], v[28:31], v[142:145], v[34:49]
	s_waitcnt lgkmcnt(0)
	v_mfma_f32_32x32x16_bf16 v[34:49], v[130:133], v[150:153], v[34:49]

.LBB0_3306:
	ds_read_b64_tr_b16 v[138:139], v203 offset:0
	ds_read_b64_tr_b16 v[140:141], v203 offset:0x800
	ds_read_b64_tr_b16 v[142:143], v203 offset:0x1000
	ds_read_b64_tr_b16 v[144:145], v203 offset:0x1800
	ds_read_b64_tr_b16 v[146:147], v203 offset:0x2000
	ds_read_b64_tr_b16 v[148:149], v203 offset:0x2800
	ds_read_b64_tr_b16 v[150:151], v203 offset:0x3000
	ds_read_b64_tr_b16 v[152:153], v203 offset:0x3800
	s_nop 0
	s_waitcnt lgkmcnt(6)
	v_mfma_f32_32x32x16_bf16 v[82:97], v[24:27], v[138:141], v[82:97]
	ds_read_b64_tr_b16 v[138:139], v203 offset:0x200
	ds_read_b64_tr_b16 v[140:141], v203 offset:0xa00
	s_waitcnt lgkmcnt(6)
	v_mfma_f32_32x32x16_bf16 v[82:97], v[28:31], v[142:145], v[82:97]
	ds_read_b64_tr_b16 v[142:143], v203 offset:0x1200
	ds_read_b64_tr_b16 v[144:145], v203 offset:0x1a00
	s_waitcnt lgkmcnt(6)
	v_mfma_f32_32x32x16_bf16 v[82:97], v[130:133], v[146:149], v[82:97]
	ds_read_b64_tr_b16 v[146:147], v203 offset:0x2200
	ds_read_b64_tr_b16 v[148:149], v203 offset:0x2a00
	ds_read_b64_tr_b16 v[154:155], v203 offset:0x3200
	ds_read_b64_tr_b16 v[156:157], v203 offset:0x3a00
	s_waitcnt lgkmcnt(8)
	v_mfma_f32_32x32x16_bf16 v[82:97], v[134:137], v[150:153], v[82:97]
	s_waitcnt lgkmcnt(6)
	v_mfma_f32_32x32x16_bf16 v[66:81], v[24:27], v[138:141], v[66:81]
	ds_read_b64_tr_b16 v[138:139], v203 offset:0x400
	ds_read_b64_tr_b16 v[140:141], v203 offset:0xc00
	s_waitcnt lgkmcnt(6)
	v_mfma_f32_32x32x16_bf16 v[66:81], v[28:31], v[142:145], v[66:81]
	ds_read_b64_tr_b16 v[142:143], v203 offset:0x1400
	ds_read_b64_tr_b16 v[144:145], v203 offset:0x1c00
	s_waitcnt lgkmcnt(6)
	v_mfma_f32_32x32x16_bf16 v[66:81], v[130:133], v[146:149], v[66:81]
	ds_read_b64_tr_b16 v[146:147], v203 offset:0x2400
	ds_read_b64_tr_b16 v[148:149], v203 offset:0x2c00
	ds_read_b64_tr_b16 v[150:151], v203 offset:0x3400
	ds_read_b64_tr_b16 v[152:153], v203 offset:0x3c00
	s_waitcnt lgkmcnt(8)
	v_mfma_f32_32x32x16_bf16 v[66:81], v[134:137], v[154:157], v[66:81]
	s_waitcnt lgkmcnt(6)
	v_mfma_f32_32x32x16_bf16 v[50:65], v[24:27], v[138:141], v[50:65]
	ds_read_b64_tr_b16 v[138:139], v203 offset:0x600
	ds_read_b64_tr_b16 v[140:141], v203 offset:0xe00
	s_waitcnt lgkmcnt(6)
	v_mfma_f32_32x32x16_bf16 v[50:65], v[28:31], v[142:145], v[50:65]
	ds_read_b64_tr_b16 v[142:143], v203 offset:0x1600
	ds_read_b64_tr_b16 v[144:145], v203 offset:0x1e00
	s_waitcnt lgkmcnt(6)
	v_mfma_f32_32x32x16_bf16 v[50:65], v[130:133], v[146:149], v[50:65]
	ds_read_b64_tr_b16 v[146:147], v203 offset:0x2600
	ds_read_b64_tr_b16 v[148:149], v203 offset:0x2e00
	ds_read_b64_tr_b16 v[154:155], v203 offset:0x3600
	ds_read_b64_tr_b16 v[156:157], v203 offset:0x3e00
	s_waitcnt lgkmcnt(8)
	v_mfma_f32_32x32x16_bf16 v[50:65], v[134:137], v[150:153], v[50:65]
	s_waitcnt lgkmcnt(6)
	v_mfma_f32_32x32x16_bf16 v[34:49], v[24:27], v[138:141], v[34:49]
	s_waitcnt lgkmcnt(4)
	v_mfma_f32_32x32x16_bf16 v[34:49], v[28:31], v[142:145], v[34:49]
	s_waitcnt lgkmcnt(2)
	v_mfma_f32_32x32x16_bf16 v[34:49], v[130:133], v[146:149], v[34:49]
	s_waitcnt lgkmcnt(0)
	v_mfma_f32_32x32x16_bf16 v[34:49], v[134:137], v[154:157], v[34:49]
	s_and_b64 vcc, exec, s[70:71]
	s_cbranch_vccnz .LBB0_3304

.LBB0_3324:
	ds_read_b64_tr_b16 v[106:107], v203 offset:0x4000
	ds_read_b64_tr_b16 v[108:109], v203 offset:0x4800
	ds_read_b64_tr_b16 v[110:111], v203 offset:0x5000
	ds_read_b64_tr_b16 v[112:113], v203 offset:0x5800
	ds_read_b64_tr_b16 v[114:115], v203 offset:0x6000
	ds_read_b64_tr_b16 v[116:117], v203 offset:0x6800
	ds_read_b64_tr_b16 v[118:119], v203 offset:0x7000
	ds_read_b64_tr_b16 v[120:121], v203 offset:0x7800
	s_nop 0
	s_waitcnt lgkmcnt(6)
	v_mfma_f32_32x32x16_bf16 v[82:97], v[24:27], v[106:109], v[82:97]
	ds_read_b64_tr_b16 v[106:107], v203 offset:0x4200
	ds_read_b64_tr_b16 v[108:109], v203 offset:0x4a00
	s_waitcnt lgkmcnt(6)
	v_mfma_f32_32x32x16_bf16 v[82:97], v[28:31], v[110:113], v[82:97]
	ds_read_b64_tr_b16 v[110:111], v203 offset:0x5200
	ds_read_b64_tr_b16 v[112:113], v203 offset:0x5a00
	s_waitcnt lgkmcnt(6)
	v_mfma_f32_32x32x16_bf16 v[82:97], v[98:101], v[114:117], v[82:97]
	ds_read_b64_tr_b16 v[114:115], v203 offset:0x6200
	ds_read_b64_tr_b16 v[116:117], v203 offset:0x6a00
	ds_read_b64_tr_b16 v[122:123], v203 offset:0x7200
	ds_read_b64_tr_b16 v[124:125], v203 offset:0x7a00
	s_waitcnt lgkmcnt(8)
	v_mfma_f32_32x32x16_bf16 v[82:97], v[102:105], v[118:121], v[82:97]
	s_waitcnt lgkmcnt(6)
	v_mfma_f32_32x32x16_bf16 v[66:81], v[24:27], v[106:109], v[66:81]
	ds_read_b64_tr_b16 v[106:107], v203 offset:0x4400
	ds_read_b64_tr_b16 v[108:109], v203 offset:0x4c00
	s_waitcnt lgkmcnt(6)
	v_mfma_f32_32x32x16_bf16 v[66:81], v[28:31], v[110:113], v[66:81]
	ds_read_b64_tr_b16 v[110:111], v203 offset:0x5400
	ds_read_b64_tr_b16 v[112:113], v203 offset:0x5c00
	s_waitcnt lgkmcnt(6)
	v_mfma_f32_32x32x16_bf16 v[66:81], v[98:101], v[114:117], v[66:81]
	ds_read_b64_tr_b16 v[114:115], v203 offset:0x6400
	ds_read_b64_tr_b16 v[116:117], v203 offset:0x6c00
	ds_read_b64_tr_b16 v[118:119], v203 offset:0x7400
	ds_read_b64_tr_b16 v[120:121], v203 offset:0x7c00
	s_waitcnt lgkmcnt(8)
	v_mfma_f32_32x32x16_bf16 v[66:81], v[102:105], v[122:125], v[66:81]
	s_waitcnt lgkmcnt(6)
	v_mfma_f32_32x32x16_bf16 v[50:65], v[24:27], v[106:109], v[50:65]
	ds_read_b64_tr_b16 v[106:107], v203 offset:0x4600
	ds_read_b64_tr_b16 v[108:109], v203 offset:0x4e00
	s_waitcnt lgkmcnt(6)
	v_mfma_f32_32x32x16_bf16 v[50:65], v[28:31], v[110:113], v[50:65]
	ds_read_b64_tr_b16 v[110:111], v203 offset:0x5600
	ds_read_b64_tr_b16 v[112:113], v203 offset:0x5e00
	s_waitcnt lgkmcnt(6)
	v_mfma_f32_32x32x16_bf16 v[50:65], v[98:101], v[114:117], v[50:65]
	ds_read_b64_tr_b16 v[114:115], v203 offset:0x6600
	ds_read_b64_tr_b16 v[116:117], v203 offset:0x6e00
	ds_read_b64_tr_b16 v[122:123], v203 offset:0x7600
	ds_read_b64_tr_b16 v[124:125], v203 offset:0x7e00
	s_waitcnt lgkmcnt(8)
	v_mfma_f32_32x32x16_bf16 v[50:65], v[102:105], v[118:121], v[50:65]
	s_waitcnt lgkmcnt(6)
	v_mfma_f32_32x32x16_bf16 v[34:49], v[24:27], v[106:109], v[34:49]
	s_waitcnt lgkmcnt(4)
	v_mfma_f32_32x32x16_bf16 v[34:49], v[28:31], v[110:113], v[34:49]
	s_waitcnt lgkmcnt(2)
	v_mfma_f32_32x32x16_bf16 v[34:49], v[98:101], v[114:117], v[34:49]
	s_waitcnt lgkmcnt(0)
	v_mfma_f32_32x32x16_bf16 v[34:49], v[102:105], v[122:125], v[34:49]
